# peersel last stage: candidate address and key arithmetic trimmed (bit-field extracts, one bitop3 for the order-preserving key): 10 instead of 14 VALU per candidate
# baseline (speedup 1.0000x reference)
; #define MFMA16(a, b, c) __builtin_amdgcn_mfma_f32_16x16x32_bf16((a), (b), (c), 0, 0, 0)
; DI void peer_select_unit(const Params& p, int unit, char* lds, const bf16x8 (&kb)[4][4]) {
;     ...
;   __syncthreads();
;   {
;     const int set = wid >> 1, kh = wid & 1;
;     bf16x8 qa[2][4];
; #pragma unroll
;     for (int mt = 0; mt < 2; ++mt)
; #pragma unroll
;       for (int kk = 0; kk < 4; ++kk) qa[mt][kk] = *(const bf16x8*)(qy + (size_t)(t0 + 16 * mt + fr) * 2048 + h * 256 + set * 128 + kk * 32 + fq * 8);
; #pragma unroll
;     for (int mt = 0; mt < 2; ++mt)
; #pragma unroll
;       for (int nj = 0; nj < 4; ++nj) {
;         f32x4 d = {0.f, 0.f, 0.f, 0.f};
; #pragma unroll
;         for (int kk = 0; kk < 4; ++kk) d = MFMA16(qa[mt][kk], kb[nj][kk], d);
; #pragma unroll
;         for (int r = 0; r < 4; ++r) sc[(set * 32 + 16 * mt + 4 * fq + r) * 132 + 64 * kh + 16 * nj + fr] = d[r];
;       }
;   }
.LBB0_1652:
	v_lshlrev_b32_e32 v64, 2, v72
	v_mov_b32_e32 v66, v206
	v_and_b32_e32 v73, 7, v72
	v_and_b32_e32 v74, 0xffffffe0, v64
	v_lshlrev_b32_e32 v64, 9, v73
	v_and_or_b32 v84, v66, 15, v74
	v_and_b32_e32 v70, 0xffffff80, v66
	v_bfe_u32 v67, v66, 4, 2
	v_lshl_add_u64 v[68:69], s[58:59], 0, v[64:65]
	v_ashrrev_i32_e32 v71, 31, v70
	v_or_b32_e32 v90, 16, v84
	v_lshl_add_u64 v[68:69], v[70:71], 1, v[68:69]
	v_lshlrev_b32_e32 v64, 4, v67
	v_ashrrev_i32_e32 v85, 31, v84
	v_ashrrev_i32_e32 v91, 31, v90
	v_lshl_add_u64 v[88:89], v[68:69], 0, v[64:65]
	v_lshlrev_b64 v[68:69], 12, v[84:85]
	v_lshlrev_b64 v[90:91], 12, v[90:91]
	v_lshl_add_u64 v[116:117], v[88:89], 0, v[68:69]
	v_lshl_add_u64 v[120:121], v[88:89], 0, v[90:91]
	s_barrier
	s_waitcnt vmcnt(0)
	v_mov_b32_e32 v68, v148
	v_mov_b32_e32 v69, v149
	v_mov_b32_e32 v70, v150
	v_mov_b32_e32 v71, v151
	v_mov_b32_e32 v76, v152
	v_mov_b32_e32 v77, v153
	v_mov_b32_e32 v78, v154
	v_mov_b32_e32 v79, v155
	v_mov_b32_e32 v92, v156
	v_mov_b32_e32 v93, v157
	v_mov_b32_e32 v94, v158
	v_mov_b32_e32 v95, v159
	v_mov_b32_e32 v96, v160
	v_mov_b32_e32 v97, v161
	v_mov_b32_e32 v98, v162
	v_mov_b32_e32 v99, v163
	v_ashrrev_i32_e32 v75, 2, v66
	v_and_b32_e32 v64, 0x4f, v66
	v_lshlrev_b32_e32 v64, 2, v64
	s_mov_b64 s[20:21], -1
	s_mov_b32 s69, 0
	v_mfma_f32_16x16x32_bf16 v[80:83], v[68:71], v[0:3], 0
	v_mfma_f32_16x16x32_bf16 v[84:87], v[68:71], v[56:59], 0
	v_mfma_f32_16x16x32_bf16 v[88:91], v[68:71], v[24:27], 0
	v_mfma_f32_16x16x32_bf16 v[68:71], v[68:71], v[44:47], 0
	v_mfma_f32_16x16x32_bf16 v[100:103], v[92:95], v[0:3], 0
	v_mfma_f32_16x16x32_bf16 v[104:107], v[92:95], v[56:59], 0
	v_mfma_f32_16x16x32_bf16 v[108:111], v[92:95], v[24:27], 0
	v_mfma_f32_16x16x32_bf16 v[80:83], v[76:79], v[4:7], v[80:83]
	v_mfma_f32_16x16x32_bf16 v[84:87], v[76:79], v[16:19], v[84:87]
	v_mfma_f32_16x16x32_bf16 v[88:91], v[76:79], v[28:31], v[88:91]
	v_mfma_f32_16x16x32_bf16 v[68:71], v[76:79], v[48:51], v[68:71]
	v_mfma_f32_16x16x32_bf16 v[76:79], v[96:99], v[4:7], v[100:103]
	v_mfma_f32_16x16x32_bf16 v[100:103], v[96:99], v[16:19], v[104:107]
	v_mfma_f32_16x16x32_bf16 v[104:107], v[96:99], v[28:31], v[108:111]
	s_nop 2
	s_nop 1
	v_mov_b32_e32 v108, v164
	v_mov_b32_e32 v109, v165
	v_mov_b32_e32 v110, v166
	v_mov_b32_e32 v111, v167
	v_mov_b32_e32 v112, v168
	v_mov_b32_e32 v113, v169
	v_mov_b32_e32 v114, v170
	v_mov_b32_e32 v115, v171
	v_mov_b32_e32 v116, v172
	v_mov_b32_e32 v117, v173
	v_mov_b32_e32 v118, v174
	v_mov_b32_e32 v119, v175
	s_nop 1
	v_mfma_f32_16x16x32_bf16 v[80:83], v[108:111], v[8:11], v[80:83]
	v_mfma_f32_16x16x32_bf16 v[84:87], v[108:111], v[20:23], v[84:87]
	v_mfma_f32_16x16x32_bf16 v[88:91], v[108:111], v[32:35], v[88:91]
	v_mfma_f32_16x16x32_bf16 v[68:71], v[108:111], v[52:55], v[68:71]
	s_nop 3
	v_mov_b32_e32 v108, v178
	v_mov_b32_e32 v109, v179
	v_mov_b32_e32 v110, v180
	v_mov_b32_e32 v111, v181
	v_add_u32_e32 v184, s90, v72
	v_min_u32_e32 v184, s68, v184
	v_lshrrev_b32_e32 v185, 3, v184
	v_lshlrev_b32_e32 v185, 17, v185
	v_and_b32_e32 v184, 7, v184
	v_lshl_or_b32 v184, v184, 9, v185
	v_mov_b32_e32 v185, 0
	v_lshl_add_u64 v[184:185], v[182:183], 0, v[184:185]
	v_mov_b32_e32 v186, 0x10000
	v_mov_b32_e32 v187, 0
	v_lshl_add_u64 v[186:187], v[184:185], 0, v[186:187]
	global_load_dwordx4 v[148:151], v[184:185], off
	global_load_dwordx4 v[152:155], v[184:185], off offset:64
	global_load_dwordx4 v[156:159], v[186:187], off
	global_load_dwordx4 v[160:163], v[186:187], off offset:64
	global_load_dwordx4 v[164:167], v[184:185], off offset:128
	global_load_dwordx4 v[168:171], v[184:185], off offset:192
	global_load_dwordx4 v[172:175], v[186:187], off offset:128
	global_load_dwordx4 v[178:181], v[186:187], off offset:192
	s_nop 1
	v_mfma_f32_16x16x32_bf16 v[80:83], v[112:115], v[12:15], v[80:83]
	v_mfma_f32_16x16x32_bf16 v[84:87], v[112:115], v[40:43], v[84:87]
	v_mfma_f32_16x16x32_bf16 v[88:91], v[112:115], v[36:39], v[88:91]
	v_mfma_f32_16x16x32_bf16 v[68:71], v[112:115], v[60:63], v[68:71]
	v_and_b32_e32 v112, 0xfffffe0, v75
	v_lshl_or_b32 v67, v67, 2, v112
	v_mul_lo_u32 v67, v67, s2
	v_add3_u32 v64, v146, v67, v64
	v_add_u32_e32 v67, 0x400, v64
	s_nop 0
	ds_write2_b32 v64, v80, v84 offset1:16
	ds_write2_b32 v64, v81, v85 offset0:132 offset1:148
	ds_write2_b32 v67, v82, v86 offset0:8 offset1:24
	ds_write2_b32 v67, v83, v87 offset0:140 offset1:156
	ds_write2_b32 v64, v88, v68 offset0:32 offset1:48
	v_mfma_f32_16x16x32_bf16 v[80:83], v[92:95], v[44:47], 0
	ds_write2_b32 v64, v89, v69 offset0:164 offset1:180
	ds_write2_b32 v67, v90, v70 offset0:40 offset1:56
	ds_write2_b32 v67, v91, v71 offset0:172 offset1:188
	v_add_u32_e32 v67, 0x2000, v64
	v_add_u32_e32 v64, 0x2400, v64
	v_mfma_f32_16x16x32_bf16 v[68:71], v[96:99], v[48:51], v[80:83]
	v_mfma_f32_16x16x32_bf16 v[76:79], v[116:119], v[8:11], v[76:79]
	v_mfma_f32_16x16x32_bf16 v[100:103], v[116:119], v[20:23], v[100:103]
	v_mfma_f32_16x16x32_bf16 v[104:107], v[116:119], v[32:35], v[104:107]
	v_mfma_f32_16x16x32_bf16 v[68:71], v[116:119], v[52:55], v[68:71]
	v_mfma_f32_16x16x32_bf16 v[76:79], v[108:111], v[12:15], v[76:79]
	v_mfma_f32_16x16x32_bf16 v[100:103], v[108:111], v[40:43], v[100:103]
	s_nop 7
	ds_write2_b32 v67, v76, v100 offset0:64 offset1:80
	ds_write2_b32 v67, v77, v101 offset0:196 offset1:212
	v_mfma_f32_16x16x32_bf16 v[104:107], v[108:111], v[36:39], v[104:107]
	ds_write2_b32 v64, v78, v102 offset0:72 offset1:88
	ds_write2_b32 v64, v79, v103 offset0:204 offset1:220
	v_mfma_f32_16x16x32_bf16 v[68:71], v[108:111], v[60:63], v[68:71]
	s_nop 7
	ds_write2_b32 v67, v104, v68 offset0:96 offset1:112
	ds_write2_b32 v67, v105, v69 offset0:228 offset1:244
	ds_write2_b32 v64, v106, v70 offset0:104 offset1:120
	ds_write2_b32 v64, v107, v71 offset0:236 offset1:252
	v_lshrrev_b32_e32 v236, 2, v66
	v_and_b32_e32 v237, 3, v66
	v_mul_u32_u24_e32 v238, 0x210, v236
	v_add_u32_e32 v238, v146, v238
	v_lshl_add_u32 v239, v237, 6, v238
	s_waitcnt lgkmcnt(0)
	s_barrier
; DI unsigned ordkey(float f) { const unsigned u = __float_as_uint(f); return (u & 0x80000000u) ? ~u : (u | 0x80000000u); }
; DI void peer_select_unit(const Params& p, int unit, char* lds, const bf16x8 (&kb)[4][4]) {
;     ...
;     const int rr = pass * 32 + (tid >> 3), part = tid & 7;
;     unsigned a[16], bq[16];
;     const float* srow = sc + rr * 132 + 16 * part;
; #pragma unroll
;     for (int j = 0; j < 4; ++j) {
;       const f32x4 v = *(const f32x4*)(srow + 4 * j);
; #pragma unroll
;       for (int e = 0; e < 4; ++e) a[4 * j + e] = (ordkey(v[e]) & ~127u) | (unsigned)(127 - (16 * part + 4 * j + e));
;     }
	ds_read_b128 v[124:127], v239 offset:0
	ds_read_b128 v[128:131], v239 offset:16
	ds_read_b128 v[132:135], v239 offset:32
	ds_read_b128 v[136:139], v239 offset:48
	ds_read_b128 v[212:215], v239 offset:256
	ds_read_b128 v[216:219], v239 offset:272
	ds_read_b128 v[220:223], v239 offset:288
	ds_read_b128 v[224:227], v239 offset:304
	v_lshlrev_b32_e32 v240, 4, v237
	v_sub_u32_e32 v241, 0x7f, v240
	v_sub_u32_e32 v242, 63, v240
	v_mov_b32_e32 v243, 0xffffff80
	v_bfrev_b32_e32 v240, 1
	s_waitcnt lgkmcnt(7)
	v_ashrrev_i32_e32 v122, 31, v124
	v_bitop3_b32 v124, v124, v122, v240 bitop3:0x1e
	v_and_or_b32 v124, v124, v243, v241
	v_ashrrev_i32_e32 v123, 31, v125
	v_bitop3_b32 v125, v125, v123, v240 bitop3:0x1e
	v_and_or_b32 v125, v125, v243, v241
	v_subrev_u32_e32 v125, 1, v125
	v_ashrrev_i32_e32 v140, 31, v126
	v_bitop3_b32 v126, v126, v140, v240 bitop3:0x1e
	v_and_or_b32 v126, v126, v243, v241
	v_subrev_u32_e32 v126, 2, v126
	v_ashrrev_i32_e32 v141, 31, v127
	v_bitop3_b32 v127, v127, v141, v240 bitop3:0x1e
	v_and_or_b32 v127, v127, v243, v241
	v_subrev_u32_e32 v127, 3, v127
	s_waitcnt lgkmcnt(6)
	v_ashrrev_i32_e32 v142, 31, v128
	v_bitop3_b32 v128, v128, v142, v240 bitop3:0x1e
	v_and_or_b32 v128, v128, v243, v241
	v_subrev_u32_e32 v128, 4, v128
	v_ashrrev_i32_e32 v143, 31, v129
	v_bitop3_b32 v129, v129, v143, v240 bitop3:0x1e
	v_and_or_b32 v129, v129, v243, v241
	v_subrev_u32_e32 v129, 5, v129
	v_ashrrev_i32_e32 v144, 31, v130
	v_bitop3_b32 v130, v130, v144, v240 bitop3:0x1e
	v_and_or_b32 v130, v130, v243, v241
	v_subrev_u32_e32 v130, 6, v130
	v_ashrrev_i32_e32 v145, 31, v131
	v_bitop3_b32 v131, v131, v145, v240 bitop3:0x1e
	v_and_or_b32 v131, v131, v243, v241
	v_subrev_u32_e32 v131, 7, v131
	s_waitcnt lgkmcnt(5)
	v_ashrrev_i32_e32 v194, 31, v132
	v_bitop3_b32 v132, v132, v194, v240 bitop3:0x1e
	v_and_or_b32 v132, v132, v243, v241
	v_subrev_u32_e32 v132, 8, v132
	v_ashrrev_i32_e32 v195, 31, v133
	v_bitop3_b32 v133, v133, v195, v240 bitop3:0x1e
	v_and_or_b32 v133, v133, v243, v241
	v_subrev_u32_e32 v133, 9, v133
	v_ashrrev_i32_e32 v196, 31, v134
	v_bitop3_b32 v134, v134, v196, v240 bitop3:0x1e
	v_and_or_b32 v134, v134, v243, v241
	v_subrev_u32_e32 v134, 10, v134
	v_ashrrev_i32_e32 v197, 31, v135
	v_bitop3_b32 v135, v135, v197, v240 bitop3:0x1e
	v_and_or_b32 v135, v135, v243, v241
	v_subrev_u32_e32 v135, 11, v135
	s_waitcnt lgkmcnt(4)
	v_ashrrev_i32_e32 v198, 31, v136
	v_bitop3_b32 v136, v136, v198, v240 bitop3:0x1e
	v_and_or_b32 v136, v136, v243, v241
	v_subrev_u32_e32 v136, 12, v136
	v_ashrrev_i32_e32 v199, 31, v137
	v_bitop3_b32 v137, v137, v199, v240 bitop3:0x1e
	v_and_or_b32 v137, v137, v243, v241
	v_subrev_u32_e32 v137, 13, v137
	v_ashrrev_i32_e32 v200, 31, v138
	v_bitop3_b32 v138, v138, v200, v240 bitop3:0x1e
	v_and_or_b32 v138, v138, v243, v241
	v_subrev_u32_e32 v138, 14, v138
	v_ashrrev_i32_e32 v201, 31, v139
	v_bitop3_b32 v139, v139, v201, v240 bitop3:0x1e
	v_and_or_b32 v139, v139, v243, v241
	v_subrev_u32_e32 v139, 15, v139
	s_waitcnt lgkmcnt(3)
	v_ashrrev_i32_e32 v202, 31, v212
	v_bitop3_b32 v212, v212, v202, v240 bitop3:0x1e
	v_and_or_b32 v212, v212, v243, v242
	v_ashrrev_i32_e32 v203, 31, v213
	v_bitop3_b32 v213, v213, v203, v240 bitop3:0x1e
	v_and_or_b32 v213, v213, v243, v242
	v_subrev_u32_e32 v213, 1, v213
	v_ashrrev_i32_e32 v204, 31, v214
	v_bitop3_b32 v214, v214, v204, v240 bitop3:0x1e
	v_and_or_b32 v214, v214, v243, v242
	v_subrev_u32_e32 v214, 2, v214
	v_ashrrev_i32_e32 v205, 31, v215
	v_bitop3_b32 v215, v215, v205, v240 bitop3:0x1e
	v_and_or_b32 v215, v215, v243, v242
	v_subrev_u32_e32 v215, 3, v215
	s_waitcnt lgkmcnt(2)
	v_ashrrev_i32_e32 v122, 31, v216
	v_bitop3_b32 v216, v216, v122, v240 bitop3:0x1e
	v_and_or_b32 v216, v216, v243, v242
	v_subrev_u32_e32 v216, 4, v216
	v_ashrrev_i32_e32 v123, 31, v217
	v_bitop3_b32 v217, v217, v123, v240 bitop3:0x1e
	v_and_or_b32 v217, v217, v243, v242
	v_subrev_u32_e32 v217, 5, v217
	v_ashrrev_i32_e32 v140, 31, v218
	v_bitop3_b32 v218, v218, v140, v240 bitop3:0x1e
	v_and_or_b32 v218, v218, v243, v242
	v_subrev_u32_e32 v218, 6, v218
	v_ashrrev_i32_e32 v141, 31, v219
	v_bitop3_b32 v219, v219, v141, v240 bitop3:0x1e
	v_and_or_b32 v219, v219, v243, v242
	v_subrev_u32_e32 v219, 7, v219
	s_waitcnt lgkmcnt(1)
	v_ashrrev_i32_e32 v142, 31, v220
	v_bitop3_b32 v220, v220, v142, v240 bitop3:0x1e
	v_and_or_b32 v220, v220, v243, v242
	v_subrev_u32_e32 v220, 8, v220
	v_ashrrev_i32_e32 v143, 31, v221
	v_bitop3_b32 v221, v221, v143, v240 bitop3:0x1e
	v_and_or_b32 v221, v221, v243, v242
	v_subrev_u32_e32 v221, 9, v221
	v_ashrrev_i32_e32 v144, 31, v222
	v_bitop3_b32 v222, v222, v144, v240 bitop3:0x1e
	v_and_or_b32 v222, v222, v243, v242
	v_subrev_u32_e32 v222, 10, v222
	v_ashrrev_i32_e32 v145, 31, v223
	v_bitop3_b32 v223, v223, v145, v240 bitop3:0x1e
	v_and_or_b32 v223, v223, v243, v242
	v_subrev_u32_e32 v223, 11, v223
	s_waitcnt lgkmcnt(0)
; DI unsigned ordkey(float f) { const unsigned u = __float_as_uint(f); return (u & 0x80000000u) ? ~u : (u | 0x80000000u); }
; #define CE_DESC(x, y) do { const unsigned mx_ = (x) > (y) ? (x) : (y); const unsigned mn_ = (x) > (y) ? (y) : (x); (x) = mx_; (y) = mn_; } while (0)
; DI void sort16_desc(unsigned (&a)[16]) {
; #pragma unroll
;   for (int k = 2; k <= 16; k <<= 1)
; #pragma unroll
;     for (int j = k >> 1; j > 0; j >>= 1)
; #pragma unroll
;       for (int i = 0; i < 16; ++i) {
;         const int l = i ^ j;
;         if (l > i) { if ((i & k) == 0) CE_DESC(a[i], a[l]); else CE_DESC(a[l], a[i]); }
;       }
; }
; DI void peer_select_unit(const Params& p, int unit, char* lds, const bf16x8 (&kb)[4][4]) {
;     ...
;     const float* srow = sc + rr * 132 + 16 * part;
; #pragma unroll
;     for (int j = 0; j < 4; ++j) {
;       const f32x4 v = *(const f32x4*)(srow + 4 * j);
; #pragma unroll
;       for (int e = 0; e < 4; ++e) a[4 * j + e] = (ordkey(v[e]) & ~127u) | (unsigned)(127 - (16 * part + 4 * j + e));
;     }
;     sort16_desc(a);
	v_ashrrev_i32_e32 v194, 31, v224
	v_bitop3_b32 v224, v224, v194, v240 bitop3:0x1e
	v_and_or_b32 v224, v224, v243, v242
	v_subrev_u32_e32 v224, 12, v224
	v_ashrrev_i32_e32 v195, 31, v225
	v_bitop3_b32 v225, v225, v195, v240 bitop3:0x1e
	v_and_or_b32 v225, v225, v243, v242
	v_subrev_u32_e32 v225, 13, v225
	v_ashrrev_i32_e32 v196, 31, v226
	v_bitop3_b32 v226, v226, v196, v240 bitop3:0x1e
	v_and_or_b32 v226, v226, v243, v242
	v_subrev_u32_e32 v226, 14, v226
	v_ashrrev_i32_e32 v197, 31, v227
	v_bitop3_b32 v227, v227, v197, v240 bitop3:0x1e
	v_and_or_b32 v227, v227, v243, v242
	v_subrev_u32_e32 v227, 15, v227
	v_max_u32_e32 v198, v124, v137
	v_min_u32_e32 v199, v124, v137
	v_max_u32_e32 v200, v212, v225
	v_min_u32_e32 v201, v212, v225
	v_max_u32_e32 v202, v125, v136
	v_min_u32_e32 v203, v125, v136
	v_max_u32_e32 v204, v213, v224
	v_min_u32_e32 v205, v213, v224
	v_max_u32_e32 v122, v126, v139
	v_min_u32_e32 v123, v126, v139
	v_max_u32_e32 v140, v214, v227
	v_min_u32_e32 v141, v214, v227
	v_max_u32_e32 v142, v127, v138
	v_min_u32_e32 v143, v127, v138
	v_max_u32_e32 v144, v215, v226
	v_min_u32_e32 v145, v215, v226
	v_max_u32_e32 v194, v128, v132
	v_min_u32_e32 v195, v128, v132
	v_max_u32_e32 v196, v216, v220
	v_min_u32_e32 v197, v216, v220
	v_max_u32_e32 v124, v129, v130
	v_min_u32_e32 v137, v129, v130
	v_max_u32_e32 v212, v217, v218
	v_min_u32_e32 v225, v217, v218
	v_max_u32_e32 v125, v131, v135
	v_min_u32_e32 v136, v131, v135
	v_max_u32_e32 v213, v219, v223
	v_min_u32_e32 v224, v219, v223
	v_max_u32_e32 v126, v133, v134
	v_min_u32_e32 v139, v133, v134
	v_max_u32_e32 v214, v221, v222
	v_min_u32_e32 v227, v221, v222
	v_max_u32_e32 v127, v198, v124
	v_min_u32_e32 v138, v198, v124
	v_max_u32_e32 v215, v200, v212
	v_min_u32_e32 v226, v200, v212
	v_max_u32_e32 v128, v202, v125
	v_min_u32_e32 v132, v202, v125
	v_max_u32_e32 v216, v204, v213
	v_min_u32_e32 v220, v204, v213
	v_max_u32_e32 v129, v122, v126
	v_min_u32_e32 v130, v122, v126
	v_max_u32_e32 v217, v140, v214
	v_min_u32_e32 v218, v140, v214
	v_max_u32_e32 v131, v142, v194
	v_min_u32_e32 v135, v142, v194
	v_max_u32_e32 v219, v144, v196
	v_min_u32_e32 v223, v144, v196
	v_max_u32_e32 v133, v137, v199
	v_min_u32_e32 v134, v137, v199
	v_max_u32_e32 v221, v225, v201
	v_min_u32_e32 v222, v225, v201
	v_max_u32_e32 v198, v195, v143
	v_min_u32_e32 v124, v195, v143
	v_max_u32_e32 v200, v197, v145
	v_min_u32_e32 v212, v197, v145
	v_max_u32_e32 v202, v139, v123
	v_min_u32_e32 v125, v139, v123
	v_max_u32_e32 v204, v227, v141
	v_min_u32_e32 v213, v227, v141
	v_max_u32_e32 v122, v136, v203
	v_min_u32_e32 v126, v136, v203
	v_max_u32_e32 v140, v224, v205
	v_min_u32_e32 v214, v224, v205
	v_max_u32_e32 v142, v127, v128
	v_min_u32_e32 v194, v127, v128
	v_max_u32_e32 v144, v215, v216
	v_min_u32_e32 v196, v215, v216
	v_max_u32_e32 v137, v129, v131
	v_min_u32_e32 v199, v129, v131
	v_max_u32_e32 v225, v217, v219
	v_min_u32_e32 v201, v217, v219
	v_max_u32_e32 v195, v135, v138
	v_min_u32_e32 v143, v135, v138
	v_max_u32_e32 v197, v223, v226
	v_min_u32_e32 v145, v223, v226
	v_max_u32_e32 v139, v133, v198
	v_min_u32_e32 v123, v133, v198
	v_max_u32_e32 v227, v221, v200
	v_min_u32_e32 v141, v221, v200
	v_max_u32_e32 v136, v132, v130
	v_min_u32_e32 v203, v132, v130
	v_max_u32_e32 v224, v220, v218
	v_min_u32_e32 v205, v220, v218
	v_max_u32_e32 v127, v202, v122
	v_min_u32_e32 v128, v202, v122
	v_max_u32_e32 v215, v204, v140
	v_min_u32_e32 v216, v204, v140
	v_max_u32_e32 v129, v126, v134
	v_min_u32_e32 v131, v126, v134
	v_max_u32_e32 v217, v214, v222
	v_min_u32_e32 v219, v214, v222
	v_max_u32_e32 v135, v124, v125
	v_min_u32_e32 v138, v124, v125
	v_max_u32_e32 v223, v212, v213
	v_min_u32_e32 v226, v212, v213
	v_max_u32_e32 v133, v142, v137
	v_min_u32_e32 v198, v142, v137
	v_max_u32_e32 v221, v144, v225
	v_min_u32_e32 v200, v144, v225
	v_max_u32_e32 v132, v194, v199
	v_min_u32_e32 v130, v194, v199
	v_max_u32_e32 v220, v196, v201
	v_min_u32_e32 v218, v196, v201
	v_max_u32_e32 v202, v195, v127
	v_min_u32_e32 v122, v195, v127
	v_max_u32_e32 v204, v197, v215
	v_min_u32_e32 v140, v197, v215
	v_max_u32_e32 v126, v143, v128
	v_min_u32_e32 v134, v143, v128
	v_max_u32_e32 v214, v145, v216
	v_min_u32_e32 v222, v145, v216
	v_max_u32_e32 v124, v139, v136
	v_min_u32_e32 v125, v139, v136
	v_max_u32_e32 v212, v227, v224
	v_min_u32_e32 v213, v227, v224
	v_max_u32_e32 v142, v123, v203
	v_min_u32_e32 v137, v123, v203
	v_max_u32_e32 v144, v141, v205
	v_min_u32_e32 v225, v141, v205
	v_max_u32_e32 v194, v129, v135
	v_min_u32_e32 v199, v129, v135
	v_max_u32_e32 v196, v217, v223
	v_min_u32_e32 v201, v217, v223
	v_max_u32_e32 v195, v131, v138
	v_min_u32_e32 v127, v131, v138
	v_max_u32_e32 v197, v219, v226
	v_min_u32_e32 v215, v219, v226
	v_max_u32_e32 v143, v132, v198
	v_min_u32_e32 v128, v132, v198
	v_max_u32_e32 v145, v220, v200
	v_min_u32_e32 v216, v220, v200
	v_max_u32_e32 v139, v130, v194
	v_min_u32_e32 v136, v130, v194
	v_max_u32_e32 v227, v218, v196
	v_min_u32_e32 v224, v218, v196
	v_max_u32_e32 v123, v202, v124
	v_min_u32_e32 v203, v202, v124
	v_max_u32_e32 v141, v204, v212
	v_min_u32_e32 v205, v204, v212
	v_max_u32_e32 v129, v126, v125
	v_min_u32_e32 v135, v126, v125
	v_max_u32_e32 v217, v214, v213
	v_min_u32_e32 v223, v214, v213
	v_max_u32_e32 v131, v142, v122
	v_min_u32_e32 v138, v142, v122
	v_max_u32_e32 v219, v144, v140
	v_min_u32_e32 v226, v144, v140
	v_max_u32_e32 v132, v137, v134
	v_min_u32_e32 v198, v137, v134
	v_max_u32_e32 v220, v225, v222
	v_min_u32_e32 v200, v225, v222
	v_max_u32_e32 v130, v195, v199
	v_min_u32_e32 v194, v195, v199
	v_max_u32_e32 v218, v197, v201
	v_min_u32_e32 v196, v197, v201
	v_max_u32_e32 v202, v143, v123
; #define CE_DESC(x, y) do { const unsigned mx_ = (x) > (y) ? (x) : (y); const unsigned mn_ = (x) > (y) ? (y) : (x); (x) = mx_; (y) = mn_; } while (0)
; DI void sort16_desc(unsigned (&a)[16]) {
; #pragma unroll
;   for (int k = 2; k <= 16; k <<= 1)
; #pragma unroll
;     for (int j = k >> 1; j > 0; j >>= 1)
; #pragma unroll
;       for (int i = 0; i < 16; ++i) {
;         const int l = i ^ j;
;         if (l > i) { if ((i & k) == 0) CE_DESC(a[i], a[l]); else CE_DESC(a[l], a[i]); }
;       }
; }
; DI void merge16_desc(unsigned (&a)[16], const unsigned (&b)[16]) {
; #pragma unroll
;   for (int i = 0; i < 16; ++i) a[i] = a[i] > b[15 - i] ? a[i] : b[15 - i];
; #pragma unroll
;   for (int j = 8; j > 0; j >>= 1)
; #pragma unroll
;     for (int i = 0; i < 16; ++i) if ((i & j) == 0) CE_DESC(a[i], a[i + j]);
; }
; DI void peer_select_unit(const Params& p, int unit, char* lds, const bf16x8 (&kb)[4][4]) {
;     ...
;     dpp16<0xB1>(bq, a); merge16_desc(a, bq);
	v_min_u32_e32 v124, v143, v123
	v_max_u32_e32 v204, v145, v141
	v_min_u32_e32 v212, v145, v141
	v_max_u32_e32 v126, v128, v203
	v_min_u32_e32 v125, v128, v203
	v_max_u32_e32 v214, v216, v205
	v_min_u32_e32 v213, v216, v205
	v_max_u32_e32 v142, v129, v131
	v_min_u32_e32 v122, v129, v131
	v_max_u32_e32 v144, v217, v219
	v_min_u32_e32 v140, v217, v219
	v_max_u32_e32 v137, v135, v138
	v_min_u32_e32 v134, v135, v138
	v_max_u32_e32 v225, v223, v226
	v_min_u32_e32 v222, v223, v226
	v_max_u32_e32 v195, v132, v130
	v_min_u32_e32 v199, v132, v130
	v_max_u32_e32 v197, v220, v218
	v_min_u32_e32 v201, v220, v218
	v_max_u32_e32 v143, v198, v194
	v_min_u32_e32 v123, v198, v194
	v_max_u32_e32 v145, v200, v196
	v_min_u32_e32 v141, v200, v196
	v_max_u32_e32 v128, v126, v124
	v_min_u32_e32 v203, v126, v124
	v_max_u32_e32 v216, v214, v212
	v_min_u32_e32 v205, v214, v212
	v_max_u32_e32 v129, v139, v125
	v_min_u32_e32 v131, v139, v125
	v_max_u32_e32 v217, v227, v213
	v_min_u32_e32 v219, v227, v213
	v_max_u32_e32 v135, v195, v136
	v_min_u32_e32 v138, v195, v136
	v_max_u32_e32 v223, v197, v224
	v_min_u32_e32 v226, v197, v224
	v_max_u32_e32 v132, v143, v199
	v_min_u32_e32 v130, v143, v199
	v_max_u32_e32 v220, v145, v201
	v_min_u32_e32 v218, v145, v201
	v_max_u32_e32 v198, v129, v142
	v_min_u32_e32 v194, v129, v142
	v_max_u32_e32 v200, v217, v144
	v_min_u32_e32 v196, v217, v144
	v_max_u32_e32 v126, v131, v122
	v_min_u32_e32 v124, v131, v122
	v_max_u32_e32 v214, v219, v140
	v_min_u32_e32 v212, v219, v140
	v_max_u32_e32 v139, v137, v135
	v_min_u32_e32 v125, v137, v135
	v_max_u32_e32 v227, v225, v223
	v_min_u32_e32 v213, v225, v223
	v_max_u32_e32 v195, v134, v138
	v_min_u32_e32 v136, v134, v138
	v_max_u32_e32 v197, v222, v226
	v_min_u32_e32 v224, v222, v226
	v_max_u32_e32 v143, v198, v203
	v_min_u32_e32 v199, v198, v203
	v_max_u32_e32 v145, v200, v205
	v_min_u32_e32 v201, v200, v205
	v_max_u32_e32 v129, v194, v126
	v_min_u32_e32 v142, v194, v126
	v_max_u32_e32 v217, v196, v214
	v_min_u32_e32 v144, v196, v214
	v_max_u32_e32 v131, v139, v124
	v_min_u32_e32 v122, v139, v124
	v_max_u32_e32 v219, v227, v212
	v_min_u32_e32 v140, v227, v212
	v_max_u32_e32 v137, v125, v195
	v_min_u32_e32 v135, v125, v195
	v_max_u32_e32 v225, v213, v197
	v_min_u32_e32 v223, v213, v197
	v_max_u32_e32 v134, v132, v136
	v_min_u32_e32 v138, v132, v136
	v_max_u32_e32 v222, v220, v224
	v_min_u32_e32 v226, v220, v224
	v_max_u32_e32 v198, v142, v131
	v_min_u32_e32 v203, v142, v131
	v_max_u32_e32 v200, v144, v219
	v_min_u32_e32 v205, v144, v219
	v_max_u32_e32 v194, v122, v137
	v_min_u32_e32 v126, v122, v137
	v_max_u32_e32 v196, v140, v225
	v_min_u32_e32 v214, v140, v225
	v_max_u32_e32 v139, v133, v215
	v_max_u32_e32 v124, v202, v141
	v_max_u32_e32 v227, v128, v218
	v_max_u32_e32 v212, v143, v226
	v_max_u32_e32 v125, v199, v222
	v_max_u32_e32 v195, v129, v223
	v_max_u32_e32 v213, v198, v214
	v_max_u32_e32 v197, v203, v196
	v_max_u32_e32 v132, v194, v205
	v_max_u32_e32 v136, v126, v200
	v_max_u32_e32 v220, v135, v217
	v_max_u32_e32 v224, v134, v201
	v_max_u32_e32 v142, v138, v145
	v_max_u32_e32 v131, v130, v216
	v_max_u32_e32 v144, v123, v204
	v_max_u32_e32 v219, v127, v221
	v_max_u32_e32 v122, v139, v132
	v_min_u32_e32 v137, v139, v132
	v_max_u32_e32 v140, v124, v136
	v_min_u32_e32 v225, v124, v136
	v_max_u32_e32 v133, v227, v220
	v_min_u32_e32 v202, v227, v220
	v_max_u32_e32 v128, v212, v224
	v_min_u32_e32 v143, v212, v224
	v_max_u32_e32 v199, v125, v142
	v_min_u32_e32 v129, v125, v142
	v_max_u32_e32 v198, v195, v131
	v_min_u32_e32 v203, v195, v131
	v_max_u32_e32 v194, v213, v144
	v_min_u32_e32 v126, v213, v144
	v_max_u32_e32 v135, v197, v219
	v_min_u32_e32 v134, v197, v219
	v_max_u32_e32 v138, v122, v199
	v_min_u32_e32 v130, v122, v199
	v_max_u32_e32 v123, v140, v198
	v_min_u32_e32 v127, v140, v198
	v_max_u32_e32 v221, v133, v194
	v_min_u32_e32 v204, v133, v194
	v_max_u32_e32 v216, v128, v135
	v_min_u32_e32 v145, v128, v135
	v_max_u32_e32 v201, v137, v129
	v_min_u32_e32 v217, v137, v129
	v_max_u32_e32 v200, v225, v203
	v_min_u32_e32 v205, v225, v203
	v_max_u32_e32 v196, v202, v126
	v_min_u32_e32 v214, v202, v126
	v_max_u32_e32 v223, v143, v134
	v_min_u32_e32 v222, v143, v134
	v_max_u32_e32 v226, v138, v221
	v_min_u32_e32 v218, v138, v221
	v_max_u32_e32 v141, v123, v216
	v_min_u32_e32 v215, v123, v216
	v_max_u32_e32 v139, v130, v204
	v_min_u32_e32 v132, v130, v204
	v_max_u32_e32 v124, v127, v145
	v_min_u32_e32 v136, v127, v145
	v_max_u32_e32 v227, v201, v196
	v_min_u32_e32 v220, v201, v196
	v_max_u32_e32 v212, v200, v223
	v_min_u32_e32 v224, v200, v223
	v_max_u32_e32 v125, v217, v214
	v_min_u32_e32 v142, v217, v214
	v_max_u32_e32 v195, v205, v222
	v_min_u32_e32 v131, v205, v222
	v_max_u32_e32 v213, v226, v141
	v_min_u32_e32 v144, v226, v141
	v_max_u32_e32 v197, v218, v215
	v_min_u32_e32 v219, v218, v215
	v_max_u32_e32 v122, v139, v124
	v_min_u32_e32 v199, v139, v124
	v_max_u32_e32 v140, v132, v136
	v_min_u32_e32 v198, v132, v136
	v_max_u32_e32 v133, v227, v212
	v_min_u32_e32 v194, v227, v212
	v_max_u32_e32 v128, v220, v224
	v_min_u32_e32 v135, v220, v224
	v_max_u32_e32 v137, v125, v195
	v_min_u32_e32 v129, v125, v195
	v_max_u32_e32 v225, v142, v131
	v_min_u32_e32 v203, v142, v131
	s_nop 1
	v_max_u32_dpp v202, v203, v213 quad_perm:[1,0,3,2] row_mask:0xf bank_mask:0xf
	v_max_u32_dpp v126, v225, v144 quad_perm:[1,0,3,2] row_mask:0xf bank_mask:0xf
	v_max_u32_dpp v143, v129, v197 quad_perm:[1,0,3,2] row_mask:0xf bank_mask:0xf
	v_max_u32_dpp v134, v137, v219 quad_perm:[1,0,3,2] row_mask:0xf bank_mask:0xf
	v_max_u32_dpp v138, v135, v122 quad_perm:[1,0,3,2] row_mask:0xf bank_mask:0xf
; #define CE_DESC(x, y) do { const unsigned mx_ = (x) > (y) ? (x) : (y); const unsigned mn_ = (x) > (y) ? (y) : (x); (x) = mx_; (y) = mn_; } while (0)
; DI void merge16_desc(unsigned (&a)[16], const unsigned (&b)[16]) {
; #pragma unroll
;   for (int i = 0; i < 16; ++i) a[i] = a[i] > b[15 - i] ? a[i] : b[15 - i];
; #pragma unroll
;   for (int j = 8; j > 0; j >>= 1)
; #pragma unroll
;     for (int i = 0; i < 16; ++i) if ((i & j) == 0) CE_DESC(a[i], a[i + j]);
; }
; template <int CTRL> DI void dpp16(unsigned (&b)[16], const unsigned (&a)[16]) {
; #pragma unroll
;   for (int s = 0; s < 16; ++s) b[s] = (unsigned)__builtin_amdgcn_update_dpp(0, (int)a[s], CTRL, 0xF, 0xF, true);
; DI void peer_select_unit(const Params& p, int unit, char* lds, const bf16x8 (&kb)[4][4]) {
;     ...
;     dpp16<0xB1>(bq, a); merge16_desc(a, bq);
;     dpp16<0x4E>(bq, a); merge16_desc(a, bq);
	v_max_u32_dpp v221, v128, v199 quad_perm:[1,0,3,2] row_mask:0xf bank_mask:0xf
	v_max_u32_dpp v123, v194, v140 quad_perm:[1,0,3,2] row_mask:0xf bank_mask:0xf
	v_max_u32_dpp v216, v133, v198 quad_perm:[1,0,3,2] row_mask:0xf bank_mask:0xf
	v_max_u32_dpp v130, v198, v133 quad_perm:[1,0,3,2] row_mask:0xf bank_mask:0xf
	v_max_u32_dpp v204, v140, v194 quad_perm:[1,0,3,2] row_mask:0xf bank_mask:0xf
	v_max_u32_dpp v127, v199, v128 quad_perm:[1,0,3,2] row_mask:0xf bank_mask:0xf
	v_max_u32_dpp v145, v122, v135 quad_perm:[1,0,3,2] row_mask:0xf bank_mask:0xf
	v_max_u32_dpp v201, v219, v137 quad_perm:[1,0,3,2] row_mask:0xf bank_mask:0xf
	v_max_u32_dpp v196, v197, v129 quad_perm:[1,0,3,2] row_mask:0xf bank_mask:0xf
	v_max_u32_dpp v200, v144, v225 quad_perm:[1,0,3,2] row_mask:0xf bank_mask:0xf
	v_max_u32_dpp v223, v213, v203 quad_perm:[1,0,3,2] row_mask:0xf bank_mask:0xf
	v_max_u32_e32 v217, v202, v130
	v_min_u32_e32 v214, v202, v130
	v_max_u32_e32 v205, v126, v204
	v_min_u32_e32 v222, v126, v204
	v_max_u32_e32 v226, v143, v127
	v_min_u32_e32 v141, v143, v127
	v_max_u32_e32 v218, v134, v145
	v_min_u32_e32 v215, v134, v145
	v_max_u32_e32 v139, v138, v201
	v_min_u32_e32 v124, v138, v201
	v_max_u32_e32 v132, v221, v196
	v_min_u32_e32 v136, v221, v196
	v_max_u32_e32 v227, v123, v200
	v_min_u32_e32 v212, v123, v200
	v_max_u32_e32 v220, v216, v223
	v_min_u32_e32 v224, v216, v223
	v_max_u32_e32 v125, v217, v139
	v_min_u32_e32 v195, v217, v139
	v_max_u32_e32 v142, v205, v132
	v_min_u32_e32 v131, v205, v132
	v_max_u32_e32 v213, v226, v227
	v_min_u32_e32 v144, v226, v227
	v_max_u32_e32 v197, v218, v220
	v_min_u32_e32 v219, v218, v220
	v_max_u32_e32 v122, v214, v124
	v_min_u32_e32 v199, v214, v124
	v_max_u32_e32 v140, v222, v136
	v_min_u32_e32 v198, v222, v136
	v_max_u32_e32 v133, v141, v212
	v_min_u32_e32 v194, v141, v212
	v_max_u32_e32 v128, v215, v224
	v_min_u32_e32 v135, v215, v224
	v_max_u32_e32 v137, v125, v213
	v_min_u32_e32 v129, v125, v213
	v_max_u32_e32 v225, v142, v197
	v_min_u32_e32 v203, v142, v197
	v_max_u32_e32 v202, v195, v144
	v_min_u32_e32 v130, v195, v144
	v_max_u32_e32 v126, v131, v219
	v_min_u32_e32 v204, v131, v219
	v_max_u32_e32 v143, v122, v133
	v_min_u32_e32 v127, v122, v133
	v_max_u32_e32 v134, v140, v128
	v_min_u32_e32 v145, v140, v128
	v_max_u32_e32 v138, v199, v194
	v_min_u32_e32 v201, v199, v194
	v_max_u32_e32 v221, v198, v135
	v_min_u32_e32 v196, v198, v135
	v_max_u32_e32 v123, v137, v225
	v_min_u32_e32 v200, v137, v225
	v_max_u32_e32 v216, v129, v203
	v_min_u32_e32 v223, v129, v203
	v_max_u32_e32 v217, v202, v126
	v_min_u32_e32 v139, v202, v126
	v_max_u32_e32 v205, v130, v204
	v_min_u32_e32 v132, v130, v204
	v_max_u32_e32 v226, v143, v134
	v_min_u32_e32 v227, v143, v134
	v_max_u32_e32 v218, v127, v145
	v_min_u32_e32 v220, v127, v145
	v_max_u32_e32 v214, v138, v221
	v_min_u32_e32 v124, v138, v221
	v_max_u32_e32 v222, v201, v196
	v_min_u32_e32 v136, v201, v196
	s_nop 1
	v_max_u32_dpp v141, v136, v123 quad_perm:[2,3,0,1] row_mask:0xf bank_mask:0xf
	v_max_u32_dpp v212, v222, v200 quad_perm:[2,3,0,1] row_mask:0xf bank_mask:0xf
	v_max_u32_dpp v215, v124, v216 quad_perm:[2,3,0,1] row_mask:0xf bank_mask:0xf
	v_max_u32_dpp v224, v214, v223 quad_perm:[2,3,0,1] row_mask:0xf bank_mask:0xf
	v_max_u32_dpp v125, v220, v217 quad_perm:[2,3,0,1] row_mask:0xf bank_mask:0xf
	v_max_u32_dpp v213, v218, v139 quad_perm:[2,3,0,1] row_mask:0xf bank_mask:0xf
	v_max_u32_dpp v142, v227, v205 quad_perm:[2,3,0,1] row_mask:0xf bank_mask:0xf
	v_max_u32_dpp v197, v226, v132 quad_perm:[2,3,0,1] row_mask:0xf bank_mask:0xf
	v_max_u32_dpp v195, v132, v226 quad_perm:[2,3,0,1] row_mask:0xf bank_mask:0xf
	v_max_u32_dpp v144, v205, v227 quad_perm:[2,3,0,1] row_mask:0xf bank_mask:0xf
	v_max_u32_dpp v131, v139, v218 quad_perm:[2,3,0,1] row_mask:0xf bank_mask:0xf
	v_max_u32_dpp v219, v217, v220 quad_perm:[2,3,0,1] row_mask:0xf bank_mask:0xf
	v_max_u32_dpp v122, v223, v214 quad_perm:[2,3,0,1] row_mask:0xf bank_mask:0xf
	v_max_u32_dpp v133, v216, v124 quad_perm:[2,3,0,1] row_mask:0xf bank_mask:0xf
	v_max_u32_dpp v140, v200, v222 quad_perm:[2,3,0,1] row_mask:0xf bank_mask:0xf
	v_max_u32_dpp v128, v123, v136 quad_perm:[2,3,0,1] row_mask:0xf bank_mask:0xf
	v_max_u32_e32 v199, v141, v195
	v_min_u32_e32 v194, v141, v195
	v_max_u32_e32 v198, v212, v144
	v_min_u32_e32 v135, v212, v144
	v_max_u32_e32 v137, v215, v131
	v_min_u32_e32 v225, v215, v131
	v_max_u32_e32 v129, v224, v219
	v_min_u32_e32 v203, v224, v219
	v_max_u32_e32 v202, v125, v122
	v_min_u32_e32 v126, v125, v122
	v_max_u32_e32 v130, v213, v133
	v_min_u32_e32 v204, v213, v133
	v_max_u32_e32 v143, v142, v140
	v_min_u32_e32 v134, v142, v140
	v_max_u32_e32 v127, v197, v128
	v_min_u32_e32 v145, v197, v128
	v_max_u32_e32 v138, v199, v202
	v_min_u32_e32 v221, v199, v202
	v_max_u32_e32 v201, v198, v130
	v_min_u32_e32 v196, v198, v130
	v_max_u32_e32 v123, v137, v143
	v_min_u32_e32 v200, v137, v143
	v_max_u32_e32 v216, v129, v127
	v_min_u32_e32 v223, v129, v127
	v_max_u32_e32 v217, v194, v126
	v_min_u32_e32 v139, v194, v126
	v_max_u32_e32 v205, v135, v204
	v_min_u32_e32 v132, v135, v204
	v_max_u32_e32 v226, v225, v134
	v_min_u32_e32 v227, v225, v134
	v_max_u32_e32 v218, v203, v145
	v_min_u32_e32 v220, v203, v145
	v_max_u32_e32 v214, v138, v123
	v_min_u32_e32 v124, v138, v123
	v_max_u32_e32 v222, v201, v216
	v_min_u32_e32 v136, v201, v216
	v_max_u32_e32 v141, v221, v200
	v_min_u32_e32 v195, v221, v200
	v_max_u32_e32 v212, v196, v223
	v_min_u32_e32 v144, v196, v223
	v_max_u32_e32 v215, v217, v226
	v_min_u32_e32 v131, v217, v226
	v_max_u32_e32 v224, v205, v218
	v_min_u32_e32 v219, v205, v218
	v_max_u32_e32 v125, v139, v227
; DI unsigned ordkey(float f) { const unsigned u = __float_as_uint(f); return (u & 0x80000000u) ? ~u : (u | 0x80000000u); }
; DI void peer_select_unit(const Params& p, int unit, char* lds, const bf16x8 (&kb)[4][4]) {
;     ...
; #pragma unroll
;     for (int s = 0; s < 2; ++s) {
;       unsigned k = 0u;
; #pragma unroll
;       for (int q = 0; q < 8; ++q) k = part == q ? a[2 * q + s] : k;
;       const int idx = 127 - (int)(k & 127u);
;       topv[rr * 16 + 2 * part + s] = sc[rr * 132 + idx]; topi[rr * 16 + 2 * part + s] = idx;
;     }
;   }
;   __syncthreads();
;   if (tid < 128) {
;     const int tok = tid >> 2, q4 = tid & 3;
;     unsigned c[16], bq[16];
; #pragma unroll
;     for (int i = 0; i < 16; ++i) {
;       const unsigned code = PEER_CAND[16 * q4 + i];
;       const float v = topv[tok * 16 + ((code >> 4) & 15)] + topv[(32 + tok) * 16 + (code & 15)];
;       c[i] = code == 0xFFu ? 0u : ((ordkey(v) & ~255u) | (255u - code));
;     }
	v_min_u32_e32 v122, v139, v227
	v_max_u32_e32 v213, v132, v220
	v_min_u32_e32 v133, v132, v220
	v_max_u32_e32 v142, v214, v222
	v_min_u32_e32 v140, v214, v222
	v_max_u32_e32 v197, v124, v136
	v_min_u32_e32 v128, v124, v136
	v_max_u32_e32 v199, v141, v212
	v_min_u32_e32 v202, v141, v212
	v_max_u32_e32 v198, v195, v144
	v_min_u32_e32 v130, v195, v144
	v_max_u32_e32 v137, v215, v224
	v_min_u32_e32 v143, v215, v224
	v_max_u32_e32 v129, v131, v219
	v_min_u32_e32 v127, v131, v219
	v_max_u32_e32 v194, v125, v213
	v_min_u32_e32 v126, v125, v213
	v_max_u32_e32 v135, v122, v133
	v_min_u32_e32 v204, v122, v133
	v_cmp_eq_u32_e32 vcc, 1, v237
	s_nop 1
	v_cndmask_b32_e32 v225, v142, v199, vcc
	v_cndmask_b32_e32 v134, v140, v202, vcc
	v_cndmask_b32_e32 v203, v197, v198, vcc
	v_cndmask_b32_e32 v145, v128, v130, vcc
	v_cmp_eq_u32_e32 vcc, 2, v237
	s_nop 1
	v_cndmask_b32_e32 v225, v225, v137, vcc
	v_cndmask_b32_e32 v134, v134, v143, vcc
	v_cndmask_b32_e32 v203, v203, v129, vcc
	v_cndmask_b32_e32 v145, v145, v127, vcc
	v_cmp_eq_u32_e32 vcc, 3, v237
	s_nop 1
	v_cndmask_b32_e32 v225, v225, v194, vcc
	v_cndmask_b32_e32 v134, v134, v126, vcc
	v_cndmask_b32_e32 v203, v203, v135, vcc
	v_cndmask_b32_e32 v145, v145, v204, vcc
	v_and_b32_e32 v240, 0x7f, v225
	v_sub_u32_e32 v228, 0x7f, v240
	v_lshl_add_u32 v225, v228, 2, v238
	ds_read_b32 v232, v225
	v_and_b32_e32 v240, 0x7f, v134
	v_sub_u32_e32 v229, 0x7f, v240
	v_lshl_add_u32 v134, v229, 2, v238
	ds_read_b32 v233, v134
	v_and_b32_e32 v240, 0x7f, v203
	v_sub_u32_e32 v230, 0x7f, v240
	v_lshl_add_u32 v203, v230, 2, v238
	ds_read_b32 v234, v203
	v_and_b32_e32 v240, 0x7f, v145
	v_sub_u32_e32 v231, 0x7f, v240
	v_lshl_add_u32 v145, v231, 2, v238
	ds_read_b32 v235, v145
	v_lshlrev_b32_e32 v239, 6, v236
	v_lshl_add_u32 v239, v237, 4, v239
	v_add_u32_e32 v239, v146, v239
	ds_write_b128 v239, v[228:231] offset:37888
	s_waitcnt lgkmcnt(1)
	ds_write_b128 v239, v[232:235] offset:33792
	v_xor_b32_e32 v66, v249, v66
	v_cmp_gt_i32_e32 vcc, s18, v66
	s_waitcnt lgkmcnt(0)
	s_barrier
	s_and_saveexec_b64 s[8:9], vcc
	s_cbranch_execz .LBB0_1651
	v_and_b32_e32 v77, 3, v66
	v_lshrrev_b32_e32 v75, 2, v66
	v_lshlrev_b32_e32 v64, 4, v77
	v_and_b32_e32 v80, 0xffff, v244
	v_lshlrev_b32_e32 v66, 6, v75
	v_lshlrev_b32_e32 v76, 4, v75
	v_cmp_eq_u32_e32 vcc, 3, v77
	v_cmp_ne_u32_e64 s[0:1], 3, v77
	v_mov_b32_e32 v82, 0
	v_lshrrev_b32_e32 v67, 2, v80
	v_and_b32_e32 v68, 15, v80
	v_lshrrev_b16_e32 v79, 8, v80
	v_and_b32_e32 v67, 60, v67
	v_lshlrev_b32_e32 v68, 2, v68
	v_lshrrev_b32_e32 v69, 2, v79
	v_and_b32_e32 v78, 15, v79
	v_add3_u32 v67, v146, v67, v66
	v_add3_u32 v68, v146, v68, v66
	v_and_b32_e32 v69, 60, v69
	v_lshlrev_b32_e32 v78, 2, v78
	v_add3_u32 v81, v146, v69, v66
	v_add3_u32 v78, v146, v78, v66
	ds_read_b32 v67, v67 offset:33792
	ds_read_b32 v69, v68 offset:35840
	ds_read_b32 v66, v81 offset:33792
	ds_read_b32 v68, v78 offset:35840
	v_mov_b32_e32 v81, 0
	v_lshlrev_b32_e32 v78, 2, v76
	v_mov_b32_e32 v83, 0
	v_mov_b32_e32 v84, 0
	v_mov_b32_e32 v85, 0
	v_mov_b32_e32 v86, 0
	v_mov_b32_e32 v87, 0
	v_mov_b32_e32 v88, 0
	v_mov_b32_e32 v89, 0
	v_mov_b32_e32 v90, 0
	v_mov_b32_e32 v91, 0
	v_mov_b32_e32 v92, 0
	v_mov_b32_e32 v93, 0
	v_mov_b32_e32 v94, 0
	s_and_saveexec_b64 s[6:7], s[0:1]
	v_add_u32_e32 v240, v146, v78
	v_bfrev_b32_e32 v241, 1
	v_bfe_u32 v82, v244, 16, 8
	v_bfe_u32 v238, v244, 20, 4
	v_bfe_u32 v239, v244, 16, 4
	v_lshl_add_u32 v238, v238, 2, v240
	v_lshl_add_u32 v239, v239, 2, v240
	ds_read_b32 v210, v238 offset:33792
	ds_read_b32 v211, v239 offset:35840
	v_bfe_u32 v81, v244, 24, 8
	v_bfe_u32 v238, v244, 28, 4
	v_bfe_u32 v239, v244, 24, 4
	v_lshl_add_u32 v238, v238, 2, v240
	v_lshl_add_u32 v239, v239, 2, v240
	ds_read_b32 v212, v238 offset:33792
	ds_read_b32 v213, v239 offset:35840
	v_bfe_u32 v84, v245, 0, 8
	v_bfe_u32 v238, v245, 4, 4
	v_bfe_u32 v239, v245, 0, 4
	v_lshl_add_u32 v238, v238, 2, v240
	v_lshl_add_u32 v239, v239, 2, v240
	ds_read_b32 v214, v238 offset:33792
	ds_read_b32 v215, v239 offset:35840
	v_bfe_u32 v83, v245, 8, 8
	v_bfe_u32 v238, v245, 12, 4
	v_bfe_u32 v239, v245, 8, 4
	v_lshl_add_u32 v238, v238, 2, v240
	v_lshl_add_u32 v239, v239, 2, v240
	ds_read_b32 v216, v238 offset:33792
	ds_read_b32 v217, v239 offset:35840
	v_bfe_u32 v86, v245, 16, 8
	v_bfe_u32 v238, v245, 20, 4
	v_bfe_u32 v239, v245, 16, 4
	v_lshl_add_u32 v238, v238, 2, v240
	v_lshl_add_u32 v239, v239, 2, v240
	ds_read_b32 v218, v238 offset:33792
	ds_read_b32 v219, v239 offset:35840
	v_bfe_u32 v85, v245, 24, 8
	v_bfe_u32 v238, v245, 28, 4
	v_bfe_u32 v239, v245, 24, 4
	v_lshl_add_u32 v238, v238, 2, v240
	v_lshl_add_u32 v239, v239, 2, v240
	ds_read_b32 v220, v238 offset:33792
	ds_read_b32 v221, v239 offset:35840
	v_bfe_u32 v88, v246, 0, 8
	v_bfe_u32 v238, v246, 4, 4
	v_bfe_u32 v239, v246, 0, 4
	v_lshl_add_u32 v238, v238, 2, v240
	v_lshl_add_u32 v239, v239, 2, v240
	ds_read_b32 v222, v238 offset:33792
	ds_read_b32 v223, v239 offset:35840
	v_bfe_u32 v87, v246, 8, 8
	v_bfe_u32 v238, v246, 12, 4
	v_bfe_u32 v239, v246, 8, 4
	v_lshl_add_u32 v238, v238, 2, v240
	v_lshl_add_u32 v239, v239, 2, v240
	ds_read_b32 v224, v238 offset:33792
	ds_read_b32 v225, v239 offset:35840
	v_bfe_u32 v90, v246, 16, 8
	v_bfe_u32 v238, v246, 20, 4
	v_bfe_u32 v239, v246, 16, 4
	v_lshl_add_u32 v238, v238, 2, v240
	v_lshl_add_u32 v239, v239, 2, v240
	ds_read_b32 v226, v238 offset:33792
	ds_read_b32 v227, v239 offset:35840
	v_bfe_u32 v89, v246, 24, 8
	v_bfe_u32 v238, v246, 28, 4
	v_bfe_u32 v239, v246, 24, 4
	v_lshl_add_u32 v238, v238, 2, v240
	v_lshl_add_u32 v239, v239, 2, v240
	ds_read_b32 v228, v238 offset:33792
	ds_read_b32 v229, v239 offset:35840
	v_bfe_u32 v92, v247, 0, 8
	v_bfe_u32 v238, v247, 4, 4
	v_bfe_u32 v239, v247, 0, 4
	v_lshl_add_u32 v238, v238, 2, v240
	v_lshl_add_u32 v239, v239, 2, v240
	ds_read_b32 v230, v238 offset:33792
	ds_read_b32 v231, v239 offset:35840
	v_bfe_u32 v91, v247, 8, 8
	v_bfe_u32 v238, v247, 12, 4
	v_bfe_u32 v239, v247, 8, 4
	v_lshl_add_u32 v238, v238, 2, v240
	v_lshl_add_u32 v239, v239, 2, v240
	ds_read_b32 v232, v238 offset:33792
	ds_read_b32 v233, v239 offset:35840
	v_bfe_u32 v94, v247, 16, 8
	v_bfe_u32 v238, v247, 20, 4
	v_bfe_u32 v239, v247, 16, 4
	v_lshl_add_u32 v238, v238, 2, v240
	v_lshl_add_u32 v239, v239, 2, v240
	ds_read_b32 v234, v238 offset:33792
	ds_read_b32 v235, v239 offset:35840
	v_bfe_u32 v70, v247, 24, 8
	v_bfe_u32 v238, v247, 28, 4
	v_bfe_u32 v239, v247, 24, 4
	v_lshl_add_u32 v238, v238, 2, v240
	v_lshl_add_u32 v239, v239, 2, v240
	ds_read_b32 v236, v238 offset:33792
	ds_read_b32 v237, v239 offset:35840
	s_waitcnt lgkmcnt(0)
; DI unsigned ordkey(float f) { const unsigned u = __float_as_uint(f); return (u & 0x80000000u) ? ~u : (u | 0x80000000u); }
; DI void peer_select_unit(const Params& p, int unit, char* lds, const bf16x8 (&kb)[4][4]) {
;     ...
;     for (int i = 0; i < 16; ++i) {
;       const unsigned code = PEER_CAND[16 * q4 + i];
;       const float v = topv[tok * 16 + ((code >> 4) & 15)] + topv[(32 + tok) * 16 + (code & 15)];
;       c[i] = code == 0xFFu ? 0u : ((ordkey(v) & ~255u) | (255u - code));
;     }
	v_add_f32_e32 v210, v210, v211
	v_ashrrev_i32_e32 v211, 31, v210
	v_bitop3_b32 v210, v210, v211, v241 bitop3:0x1e
	v_and_b32_e32 v210, 0xffffff00, v210
	v_bitop3_b32 v82, v210, s19, v82 bitop3:0x36
	v_add_f32_e32 v212, v212, v213
	v_ashrrev_i32_e32 v213, 31, v212
	v_bitop3_b32 v212, v212, v213, v241 bitop3:0x1e
	v_and_b32_e32 v212, 0xffffff00, v212
	v_bitop3_b32 v81, v212, s19, v81 bitop3:0x36
	v_add_f32_e32 v214, v214, v215
	v_ashrrev_i32_e32 v215, 31, v214
	v_bitop3_b32 v214, v214, v215, v241 bitop3:0x1e
	v_and_b32_e32 v214, 0xffffff00, v214
	v_bitop3_b32 v84, v214, s19, v84 bitop3:0x36
	v_add_f32_e32 v216, v216, v217
	v_ashrrev_i32_e32 v217, 31, v216
	v_bitop3_b32 v216, v216, v217, v241 bitop3:0x1e
	v_and_b32_e32 v216, 0xffffff00, v216
	v_bitop3_b32 v83, v216, s19, v83 bitop3:0x36
	v_add_f32_e32 v218, v218, v219
	v_ashrrev_i32_e32 v219, 31, v218
	v_bitop3_b32 v218, v218, v219, v241 bitop3:0x1e
	v_and_b32_e32 v218, 0xffffff00, v218
	v_bitop3_b32 v86, v218, s19, v86 bitop3:0x36
	v_add_f32_e32 v220, v220, v221
	v_ashrrev_i32_e32 v221, 31, v220
	v_bitop3_b32 v220, v220, v221, v241 bitop3:0x1e
	v_and_b32_e32 v220, 0xffffff00, v220
	v_bitop3_b32 v85, v220, s19, v85 bitop3:0x36
	v_add_f32_e32 v222, v222, v223
	v_ashrrev_i32_e32 v223, 31, v222
	v_bitop3_b32 v222, v222, v223, v241 bitop3:0x1e
	v_and_b32_e32 v222, 0xffffff00, v222
	v_bitop3_b32 v88, v222, s19, v88 bitop3:0x36
	v_add_f32_e32 v224, v224, v225
	v_ashrrev_i32_e32 v225, 31, v224
	v_bitop3_b32 v224, v224, v225, v241 bitop3:0x1e
	v_and_b32_e32 v224, 0xffffff00, v224
	v_bitop3_b32 v87, v224, s19, v87 bitop3:0x36
	v_add_f32_e32 v226, v226, v227
	v_ashrrev_i32_e32 v227, 31, v226
	v_bitop3_b32 v226, v226, v227, v241 bitop3:0x1e
	v_and_b32_e32 v226, 0xffffff00, v226
	v_bitop3_b32 v90, v226, s19, v90 bitop3:0x36
	v_add_f32_e32 v228, v228, v229
	v_ashrrev_i32_e32 v229, 31, v228
	v_bitop3_b32 v228, v228, v229, v241 bitop3:0x1e
	v_and_b32_e32 v228, 0xffffff00, v228
	v_bitop3_b32 v89, v228, s19, v89 bitop3:0x36
	v_add_f32_e32 v230, v230, v231
	v_ashrrev_i32_e32 v231, 31, v230
	v_bitop3_b32 v230, v230, v231, v241 bitop3:0x1e
	v_and_b32_e32 v230, 0xffffff00, v230
	v_bitop3_b32 v92, v230, s19, v92 bitop3:0x36
	v_add_f32_e32 v232, v232, v233
	v_ashrrev_i32_e32 v233, 31, v232
	v_bitop3_b32 v232, v232, v233, v241 bitop3:0x1e
	v_and_b32_e32 v232, 0xffffff00, v232
	v_bitop3_b32 v91, v232, s19, v91 bitop3:0x36
	v_add_f32_e32 v234, v234, v235
	v_ashrrev_i32_e32 v235, 31, v234
	v_bitop3_b32 v234, v234, v235, v241 bitop3:0x1e
	v_and_b32_e32 v234, 0xffffff00, v234
	v_bitop3_b32 v94, v234, s19, v94 bitop3:0x36
	v_add_f32_e32 v236, v236, v237
	v_ashrrev_i32_e32 v237, 31, v236
	v_bitop3_b32 v236, v236, v237, v241 bitop3:0x1e
	v_and_b32_e32 v236, 0xffffff00, v236
	v_bitop3_b32 v93, v236, s19, v70 bitop3:0x36
	s_or_b64 exec, exec, s[6:7]
	s_mov_b64 s[4:5], exec
	s_branch .LBB0_1650
